# v76 + SWA tile loop: O accumulators rescaled in place (temp v128), the 32 per-iteration phi copies v[86:117]<-v[2:33] at the back-edge removed
# baseline (speedup 1.0000x reference)
.LBB0_3628:
	v_cmp_lt_f32_e32 vcc, s62, v0
	s_cbranch_vccz .LBB0_3630
	v_max_f32_e32 v0, v0, v0
	v_max_f32_e32 v128, 0, v0
	v_exp_f32_e64 v0, -v128
	v_add_f32_e32 v121, v121, v128
	v_sub_f32_e32 v49, v49, v128
	v_sub_f32_e32 v48, v48, v128
	v_mul_f32_e32 v120, v120, v0
	v_sub_f32_e32 v47, v47, v128
	v_sub_f32_e32 v46, v46, v128
	v_sub_f32_e32 v45, v45, v128
	v_sub_f32_e32 v44, v44, v128
	v_sub_f32_e32 v43, v43, v128
	v_sub_f32_e32 v42, v42, v128
	v_sub_f32_e32 v41, v41, v128
	v_sub_f32_e32 v40, v40, v128
	v_sub_f32_e32 v39, v39, v128
	v_sub_f32_e32 v38, v38, v128
	v_sub_f32_e32 v37, v37, v128
	v_sub_f32_e32 v36, v36, v128
	v_sub_f32_e32 v35, v35, v128
	v_sub_f32_e32 v34, v34, v128
	v_sub_f32_e32 v65, v65, v128
	v_sub_f32_e32 v64, v64, v128
	v_sub_f32_e32 v63, v63, v128
	v_sub_f32_e32 v62, v62, v128
	v_sub_f32_e32 v61, v61, v128
	v_sub_f32_e32 v60, v60, v128
	v_sub_f32_e32 v59, v59, v128
	v_sub_f32_e32 v58, v58, v128
	v_sub_f32_e32 v57, v57, v128
	v_sub_f32_e32 v56, v56, v128
	v_sub_f32_e32 v55, v55, v128
	v_sub_f32_e32 v54, v54, v128
	v_sub_f32_e32 v53, v53, v128
	v_sub_f32_e32 v52, v52, v128
	v_sub_f32_e32 v51, v51, v128
	v_sub_f32_e32 v50, v50, v128
	v_pk_mul_f32 v[32:33], v[32:33], v[0:1] op_sel_hi:[1,0]
	v_pk_mul_f32 v[30:31], v[30:31], v[0:1] op_sel_hi:[1,0]
	v_pk_mul_f32 v[28:29], v[28:29], v[0:1] op_sel_hi:[1,0]
	v_pk_mul_f32 v[26:27], v[26:27], v[0:1] op_sel_hi:[1,0]
	v_pk_mul_f32 v[24:25], v[24:25], v[0:1] op_sel_hi:[1,0]
	v_pk_mul_f32 v[22:23], v[22:23], v[0:1] op_sel_hi:[1,0]
	v_pk_mul_f32 v[20:21], v[20:21], v[0:1] op_sel_hi:[1,0]
	v_pk_mul_f32 v[18:19], v[18:19], v[0:1] op_sel_hi:[1,0]
	v_pk_mul_f32 v[16:17], v[16:17], v[0:1] op_sel_hi:[1,0]
	v_pk_mul_f32 v[14:15], v[14:15], v[0:1] op_sel_hi:[1,0]
	v_pk_mul_f32 v[12:13], v[12:13], v[0:1] op_sel_hi:[1,0]
	v_pk_mul_f32 v[10:11], v[10:11], v[0:1] op_sel_hi:[1,0]
	v_pk_mul_f32 v[8:9], v[8:9], v[0:1] op_sel_hi:[1,0]
	v_pk_mul_f32 v[6:7], v[6:7], v[0:1] op_sel_hi:[1,0]
	v_pk_mul_f32 v[4:5], v[4:5], v[0:1] op_sel_hi:[1,0]
	v_pk_mul_f32 v[2:3], v[2:3], v[0:1] op_sel_hi:[1,0]
.LBB0_3630:
	v_exp_f32_e32 v0, v34
	v_exp_f32_e32 v90, v50
	v_exp_f32_e32 v91, v35
	v_exp_f32_e32 v92, v51
	v_exp_f32_e32 v93, v36
	v_exp_f32_e32 v94, v52
	v_exp_f32_e32 v95, v37
	v_exp_f32_e32 v96, v53
	v_add_f32_e32 v34, 0, v0
	v_add_f32_e32 v50, 0, v90
	v_add_f32_e32 v34, v91, v34
	v_add_f32_e32 v35, v92, v50
	v_add_f32_e32 v34, v93, v34
	v_add_f32_e32 v36, v94, v35
	v_add_f32_e32 v35, v95, v34
	v_add_f32_e32 v34, v96, v36
	v_exp_f32_e32 v37, v38
	v_exp_f32_e32 v36, v54
	v_exp_f32_e32 v39, v39
	v_exp_f32_e32 v38, v55
	v_exp_f32_e32 v51, v40
	v_exp_f32_e32 v50, v56
	v_exp_f32_e32 v41, v41
	v_exp_f32_e32 v40, v57
	v_exp_f32_e32 v53, v42
	v_exp_f32_e32 v52, v58
	v_pk_add_f32 v[34:35], v[36:37], v[34:35]
	v_exp_f32_e32 v55, v43
	v_exp_f32_e32 v54, v59
	v_pk_add_f32 v[34:35], v[38:39], v[34:35]
	v_exp_f32_e32 v57, v44
	v_exp_f32_e32 v56, v60
	v_pk_add_f32 v[34:35], v[50:51], v[34:35]
	v_exp_f32_e32 v59, v45
	v_exp_f32_e32 v58, v61
	v_pk_add_f32 v[34:35], v[40:41], v[34:35]
	v_exp_f32_e32 v61, v46
	v_exp_f32_e32 v60, v62
	v_pk_add_f32 v[34:35], v[52:53], v[34:35]
	v_exp_f32_e32 v87, v47
	v_exp_f32_e32 v86, v63
	v_pk_add_f32 v[34:35], v[54:55], v[34:35]
	v_exp_f32_e32 v63, v48
	v_exp_f32_e32 v62, v64
	v_exp_f32_e32 v89, v49
	v_exp_f32_e32 v88, v65
	v_pk_add_f32 v[34:35], v[56:57], v[34:35]
	v_cvt_pk_bf16_f32 v46, v0, v91
	v_pk_add_f32 v[34:35], v[58:59], v[34:35]
	v_add_u32_e32 v0, s0, v125
	v_pk_add_f32 v[34:35], v[60:61], v[34:35]
	v_add3_u32 v0, v0, v126, v122
	v_pk_add_f32 v[34:35], v[86:87], v[34:35]
	v_cvt_pk_bf16_f32 v49, v51, v41
	v_pk_add_f32 v[34:35], v[62:63], v[34:35]
	v_cvt_pk_bf16_f32 v45, v63, v89
	v_cvt_pk_bf16_f32 v41, v62, v88
	s_waitcnt vmcnt(0)
	ds_read_b64_tr_b16 v[62:63], v0 offset:16384
	ds_read_b64_tr_b16 v[64:65], v0 offset:16896
	v_pk_add_f32 v[34:35], v[88:89], v[34:35]
	v_cvt_pk_bf16_f32 v47, v93, v95
	v_add_f32_e32 v34, v34, v35
	v_cvt_pk_bf16_f32 v48, v37, v39
	v_cvt_pk_bf16_f32 v44, v61, v87
	v_cvt_pk_bf16_f32 v37, v50, v40
	v_cvt_pk_bf16_f32 v40, v60, v86
	ds_read_b64_tr_b16 v[86:87], v0 offset:17408
	ds_read_b64_tr_b16 v[88:89], v0 offset:17920
	v_add_f32_e32 v120, v120, v34
	v_cvt_pk_bf16_f32 v34, v90, v92
	ds_read_b64_tr_b16 v[90:91], v0 offset:18432
	ds_read_b64_tr_b16 v[92:93], v0 offset:18944
	s_waitcnt lgkmcnt(4)
	v_mfma_f32_32x32x16_bf16 v[2:17], v[62:65], v[46:49], v[2:17]
	v_cvt_pk_bf16_f32 v42, v53, v55
	v_cvt_pk_bf16_f32 v43, v57, v59
	v_cvt_pk_bf16_f32 v35, v94, v96
	ds_read_b64_tr_b16 v[94:95], v0 offset:19456
	ds_read_b64_tr_b16 v[96:97], v0 offset:19968
	v_cvt_pk_bf16_f32 v36, v36, v38
	v_cvt_pk_bf16_f32 v38, v52, v54
	s_waitcnt lgkmcnt(4)
	v_mfma_f32_32x32x16_bf16 v[2:17], v[86:89], v[42:45], v[2:17]
	ds_read_b64_tr_b16 v[98:99], v0 offset:20480
	ds_read_b64_tr_b16 v[100:101], v0 offset:20992
	v_cvt_pk_bf16_f32 v39, v56, v58
	s_xor_b32 s2, s2, 1
	s_cmp_lt_i32 s47, 0
	s_waitcnt lgkmcnt(4)
	v_mfma_f32_32x32x16_bf16 v[2:17], v[90:93], v[34:37], v[2:17]
	ds_read_b64_tr_b16 v[58:59], v0 offset:21504
	ds_read_b64_tr_b16 v[60:61], v0 offset:22016
	s_waitcnt lgkmcnt(4)
	v_mfma_f32_32x32x16_bf16 v[2:17], v[94:97], v[38:41], v[2:17]
	ds_read_b64_tr_b16 v[50:51], v0 offset:22528
	ds_read_b64_tr_b16 v[52:53], v0 offset:23040
	s_waitcnt lgkmcnt(4)
	v_mfma_f32_32x32x16_bf16 v[18:33], v[98:101], v[46:49], v[18:33]
	ds_read_b64_tr_b16 v[54:55], v0 offset:23552
	ds_read_b64_tr_b16 v[56:57], v0 offset:24064
	s_waitcnt lgkmcnt(4)
	v_mfma_f32_32x32x16_bf16 v[18:33], v[58:61], v[42:45], v[18:33]
	s_waitcnt lgkmcnt(2)
	v_mfma_f32_32x32x16_bf16 v[18:33], v[50:53], v[34:37], v[18:33]
	s_waitcnt lgkmcnt(0)
	v_mfma_f32_32x32x16_bf16 v[18:33], v[54:57], v[38:41], v[18:33]
	s_cbranch_scc1 .LBB0_3633
	s_mov_b32 s8, s47
	s_branch .LBB0_3619
